# baseline (speedup 1.0000x reference)
.LBB0_55:
	s_waitcnt lgkmcnt(14)
	v_mfma_f32_16x16x32_f16 v[102:105], v[30:33], v[82:85], 0
	s_mul_i32 s40, s3, 13
	s_add_i32 s6, s42, s40
	s_lshl_b32 s6, s6, 8
	s_waitcnt lgkmcnt(11)
	v_mfma_f32_16x16x32_f16 v[110:113], v[46:49], v[82:85], 0
	s_lshl_b32 s38, s33, 6
	s_or_b32 s6, s6, s38
	v_mul_u32_u24_e32 v186, 0x650, v206
	s_waitcnt lgkmcnt(7)
	v_mfma_f32_16x16x32_f16 v[162:165], v[54:57], v[82:85], 0
	v_cmp_eq_u32_e64 s[14:15], 0, v1
	s_waitcnt lgkmcnt(3)
	v_mfma_f32_16x16x32_f16 v[82:85], v[62:65], v[82:85], 0
	v_mfma_f32_16x16x32_f16 v[102:105], v[22:25], v[78:81], v[102:105]
	v_mfma_f32_16x16x32_f16 v[110:113], v[34:37], v[78:81], v[110:113]
	v_mfma_f32_16x16x32_f16 v[162:165], v[50:53], v[78:81], v[162:165]
	s_waitcnt lgkmcnt(2)
	v_mfma_f32_16x16x32_f16 v[78:81], v[58:61], v[78:81], v[82:85]
	v_mfma_f32_16x16x32_f16 v[82:85], v[18:21], v[74:77], v[102:105]
	v_mfma_f32_16x16x32_f16 v[102:105], v[26:29], v[74:77], v[110:113]
	v_mfma_f32_16x16x32_f16 v[110:113], v[38:41], v[74:77], v[162:165]
	s_waitcnt lgkmcnt(1)
	v_mfma_f32_16x16x32_f16 v[74:77], v[42:45], v[74:77], v[78:81]
	s_nop 0
	v_or_b32_e32 v162, s6, v1
	v_mfma_f32_16x16x32_f16 v[78:81], v[14:17], v[70:73], v[82:85]
	v_mfma_f32_16x16x32_f16 v[82:85], v[2:5], v[70:73], v[102:105]
	v_mfma_f32_16x16x32_f16 v[102:105], v[6:9], v[70:73], v[110:113]
	s_nop 5
	v_max_f32_e32 v89, v79, v79
	v_max_f32_e32 v163, v78, v78
	v_max_f32_e32 v89, v163, v89
	v_max3_f32 v89, v89, v80, v81
	v_max3_f32 v89, v89, v82, v83
	s_waitcnt lgkmcnt(0)
	v_mfma_f32_16x16x32_f16 v[70:73], v[10:13], v[70:73], v[74:77]
	v_max3_f32 v89, v89, v84, v85
	v_max3_f32 v89, v89, v102, v103
	v_max3_f32 v89, v89, v104, v105
	v_ashrrev_i32_e32 v163, 31, v162
	s_nop 3
	v_max3_f32 v74, v89, v70, v71
	v_max3_f32 v74, v74, v72, v73
	v_mov_b32_e32 v75, v74
	s_nop 1
	v_permlane16_swap_b32_e32 v74, v75
	v_max_f32_e32 v75, v75, v75
	v_max_f32_e32 v74, v74, v74
	v_max_f32_e32 v74, v74, v75
	v_mov_b32_e32 v75, v74
	s_nop 1
	v_permlane32_swap_b32_e32 v74, v75
	v_max_f32_e32 v75, v75, v75
	v_max_f32_e32 v74, v74, v74
	v_max_f32_e32 v74, v74, v75
	v_mul_f32_e32 v89, 0xbfb8aa3b, v74
	v_fmamk_f32 v74, v78, 0x3fb8aa3b, v89
	v_exp_f32_e32 v74, v74
	v_fmamk_f32 v75, v79, 0x3fb8aa3b, v89
	v_exp_f32_e32 v75, v75
	v_fmamk_f32 v76, v80, 0x3fb8aa3b, v89
	v_exp_f32_e32 v76, v76
	v_fmamk_f32 v77, v81, 0x3fb8aa3b, v89
	v_exp_f32_e32 v77, v77
	v_add_f32_e32 v78, 0, v74
	v_add_f32_e32 v78, v75, v78
	v_add_f32_e32 v78, v76, v78
	v_add_f32_e32 v110, v77, v78
	v_fmamk_f32 v78, v82, 0x3fb8aa3b, v89
	v_exp_f32_e32 v78, v78
	v_fmamk_f32 v79, v83, 0x3fb8aa3b, v89
	v_exp_f32_e32 v79, v79
	v_fmamk_f32 v80, v84, 0x3fb8aa3b, v89
	v_exp_f32_e32 v80, v80
	v_fmamk_f32 v81, v85, 0x3fb8aa3b, v89
	v_exp_f32_e32 v81, v81
	v_add_f32_e32 v82, v78, v110
	v_add_f32_e32 v82, v79, v82
	v_add_f32_e32 v82, v80, v82
	v_add_f32_e32 v110, v81, v82
	v_fmamk_f32 v82, v102, 0x3fb8aa3b, v89
	v_exp_f32_e32 v82, v82
	v_fmamk_f32 v83, v103, 0x3fb8aa3b, v89
	v_exp_f32_e32 v83, v83
	v_fmamk_f32 v84, v104, 0x3fb8aa3b, v89
	v_exp_f32_e32 v84, v84
	v_fmamk_f32 v85, v105, 0x3fb8aa3b, v89
	v_exp_f32_e32 v85, v85
	v_fmamk_f32 v70, v70, 0x3fb8aa3b, v89
	v_add_f32_e32 v102, v82, v110
	v_exp_f32_e32 v70, v70
	v_fmamk_f32 v71, v71, 0x3fb8aa3b, v89
	v_add_f32_e32 v102, v83, v102
	v_exp_f32_e32 v71, v71
	v_fmamk_f32 v72, v72, 0x3fb8aa3b, v89
	v_add_f32_e32 v102, v84, v102
	v_exp_f32_e32 v72, v72
	v_fmac_f32_e32 v89, 0x3fb8aa3b, v73
	v_add_f32_e32 v102, v85, v102
	v_exp_f32_e32 v73, v89
	v_add_f32_e32 v89, v70, v102
	v_add_f32_e32 v89, v71, v89
	v_add_f32_e32 v89, v72, v89
	v_add_f32_e32 v89, v73, v89
	v_mov_b32_e32 v102, v89
	s_nop 1
	v_permlane16_swap_b32_e32 v89, v102
	v_add_f32_e32 v89, v89, v102
	v_mov_b32_e32 v102, v89
	s_nop 1
	v_permlane32_swap_b32_e32 v89, v102
	v_add_f32_e32 v89, v89, v102
	v_rcp_f32_e32 v102, v89
	v_lshl_add_u64 v[104:105], v[162:163], 4, s[20:21]
	global_store_dwordx4 v[104:105], v[66:69], off sc1
	s_nop 1
	v_pk_mul_f32 v[66:67], v[102:103], v[74:75] op_sel_hi:[0,1]
	v_pk_mul_f32 v[68:69], v[102:103], v[76:77] op_sel_hi:[0,1]
	v_cvt_pk_f16_f32 v66, v66, v67
	v_cvt_pk_f16_f32 v67, v68, v69
	v_lshl_add_u32 v74, v87, 3, v186
	ds_write_b64 v74, v[66:67]
	v_pk_mul_f32 v[66:67], v[102:103], v[78:79] op_sel_hi:[0,1]
	v_pk_mul_f32 v[68:69], v[102:103], v[80:81] op_sel_hi:[0,1]
	v_cvt_pk_f16_f32 v66, v66, v67
	v_cvt_pk_f16_f32 v67, v68, v69
	ds_write_b64 v74, v[66:67] offset:6464
	v_pk_mul_f32 v[66:67], v[102:103], v[82:83] op_sel_hi:[0,1]
	v_pk_mul_f32 v[68:69], v[102:103], v[84:85] op_sel_hi:[0,1]
	v_cvt_pk_f16_f32 v66, v66, v67
	v_cvt_pk_f16_f32 v67, v68, v69
	ds_write_b64 v74, v[66:67] offset:12928
	v_pk_mul_f32 v[66:67], v[102:103], v[70:71] op_sel_hi:[0,1]
	v_pk_mul_f32 v[68:69], v[102:103], v[72:73] op_sel_hi:[0,1]
	v_cvt_pk_f16_f32 v66, v66, v67
	v_cvt_pk_f16_f32 v67, v68, v69
	ds_write_b64 v74, v[66:67] offset:19392
	s_waitcnt lgkmcnt(0)
	s_and_saveexec_b64 s[6:7], s[14:15]
	s_lshl_b32 s25, s42, 2
	s_add_i32 s25, s25, 0x14a00
	v_mov_b32_e32 v66, 1
	v_mov_b32_e32 v67, s25
	ds_write_b32 v67, v66
	s_or_b64 exec, exec, s[6:7]
	s_waitcnt vmcnt(11)
	v_ashrrev_i32_e32 v89, 31, v88
	v_or_b32_e32 v82, 0xc0, v87
	v_lshlrev_b64 v[66:67], 9, v[88:89]
	v_min_u32_e32 v82, 0xc7, v82
	v_lshl_add_u64 v[66:67], s[12:13], 0, v[66:67]
	v_lshlrev_b32_e32 v180, 2, v205
	v_mov_b32_e32 v181, 0
	v_add_u32_e32 v82, s37, v82
	v_lshl_add_u64 v[78:79], v[66:67], 0, v[180:181]
	v_ashrrev_i32_e32 v83, 31, v82
	global_load_dwordx4 v[174:177], v[78:79], off
	global_load_dwordx4 v[170:173], v[78:79], off offset:64
	global_load_dwordx4 v[166:169], v[78:79], off offset:128
	global_load_dwordx4 v[162:165], v[78:79], off offset:192
	global_load_dwordx4 v[66:69], v[78:79], off offset:256
	global_load_dwordx4 v[70:73], v[78:79], off offset:320
	global_load_dwordx4 v[74:77], v[78:79], off offset:384
	s_nop 0
	global_load_dwordx4 v[78:81], v[78:79], off offset:448
	v_lshl_add_u64 v[82:83], v[82:83], 2, s[8:9]
	s_waitcnt vmcnt(18)
	v_ashrrev_i32_e32 v87, 31, v86
	global_load_dword v182, v[82:83], off
	v_lshlrev_b64 v[82:83], 9, v[86:87]
	v_lshl_add_u64 v[82:83], s[12:13], 0, v[82:83]
	v_lshl_add_u64 v[184:185], v[82:83], 0, v[180:181]
	global_load_dwordx4 v[110:113], v[184:185], off
	global_load_dwordx4 v[102:105], v[184:185], off offset:64
	global_load_dwordx4 v[86:89], v[184:185], off offset:128
	global_load_dwordx4 v[82:85], v[184:185], off offset:192
	v_cvt_pk_f16_f32 v142, v142, v143
	v_cvt_pk_f16_f32 v143, v144, v145
	v_cvt_pk_f16_f32 v144, v138, v139
	v_cvt_pk_f16_f32 v145, v140, v141
	v_cvt_pk_f16_f32 v134, v134, v135
	v_cvt_pk_f16_f32 v135, v136, v137
	v_cvt_pk_f16_f32 v136, v130, v131
	v_cvt_pk_f16_f32 v137, v132, v133
	v_cvt_pk_f16_f32 v122, v122, v123
	v_cvt_pk_f16_f32 v123, v124, v125
	v_cvt_pk_f16_f32 v124, v118, v119
	v_cvt_pk_f16_f32 v125, v120, v121
	v_cvt_pk_f16_f32 v118, v90, v91
	v_cvt_pk_f16_f32 v119, v92, v93
	v_cvt_pk_f16_f32 v120, v94, v95
	v_cvt_pk_f16_f32 v121, v96, v97
	v_cndmask_b32_e64 v90, 0, 1, s[10:11]
	v_cmp_ne_u32_e64 s[6:7], 1, v90
	v_mov_b64_e32 v[90:91], v[142:143]
	s_andn2_b64 vcc, exec, s[10:11]
	v_mov_b64_e32 v[92:93], v[144:145]
	s_cbranch_vccnz .LBB0_59
	s_cmp_eq_u32 s33, 1
	s_cselect_b64 vcc, -1, 0
	s_cmp_eq_u32 s33, 2
	s_cselect_b64 s[8:9], -1, 0
	v_cndmask_b32_e64 v90, v118, v122, s[8:9]
	v_cndmask_b32_e64 v91, v119, v123, s[8:9]
	v_cndmask_b32_e64 v92, v120, v124, s[8:9]
	v_cndmask_b32_e64 v93, v121, v125, s[8:9]
	v_cndmask_b32_e32 v93, v93, v137, vcc
	v_cndmask_b32_e32 v92, v92, v136, vcc
	v_cndmask_b32_e32 v91, v91, v135, vcc
	v_cndmask_b32_e32 v90, v90, v134, vcc
.LBB0_59:
	v_mfma_f32_16x16x32_f16 v[94:97], v[30:33], v[142:145], 0
	s_add_i32 s8, s24, s40
	s_lshl_b32 s8, s8, 8
	s_or_b32 s8, s8, s38
	v_mfma_f32_16x16x32_f16 v[130:133], v[46:49], v[142:145], 0
	v_mfma_f32_16x16x32_f16 v[94:97], v[22:25], v[134:137], v[94:97]
	v_mfma_f32_16x16x32_f16 v[138:141], v[54:57], v[142:145], 0
	v_mfma_f32_16x16x32_f16 v[130:133], v[34:37], v[134:137], v[130:133]
	v_mfma_f32_16x16x32_f16 v[142:145], v[62:65], v[142:145], 0
	v_mfma_f32_16x16x32_f16 v[94:97], v[18:21], v[122:125], v[94:97]
	v_mfma_f32_16x16x32_f16 v[138:141], v[50:53], v[134:137], v[138:141]
	v_mfma_f32_16x16x32_f16 v[130:133], v[26:29], v[122:125], v[130:133]
	v_mfma_f32_16x16x32_f16 v[134:137], v[58:61], v[134:137], v[142:145]
	v_mfma_f32_16x16x32_f16 v[94:97], v[14:17], v[118:121], v[94:97]
	s_nop 2
	v_or_b32_e32 v142, s8, v1
	v_mfma_f32_16x16x32_f16 v[138:141], v[38:41], v[122:125], v[138:141]
	v_mfma_f32_16x16x32_f16 v[130:133], v[2:5], v[118:121], v[130:133]
	v_mfma_f32_16x16x32_f16 v[122:125], v[42:45], v[122:125], v[134:137]
	s_nop 2
	v_max_f32_e32 v134, v95, v95
	v_max_f32_e32 v135, v94, v94
	v_max_f32_e32 v134, v135, v134
	v_max3_f32 v134, v134, v96, v97
	v_max3_f32 v143, v134, v130, v131
	v_mfma_f32_16x16x32_f16 v[134:137], v[6:9], v[118:121], v[138:141]
	v_mfma_f32_16x16x32_f16 v[118:121], v[10:13], v[118:121], v[122:125]
	s_nop 1
	v_max3_f32 v138, v143, v132, v133
	s_nop 3
	v_max3_f32 v138, v138, v134, v135
	v_max3_f32 v138, v138, v136, v137
	v_ashrrev_i32_e32 v143, 31, v142
	v_max3_f32 v122, v138, v118, v119
	v_max3_f32 v122, v122, v120, v121
	v_mov_b32_e32 v123, v122
	s_nop 1
	v_permlane16_swap_b32_e32 v122, v123
	v_max_f32_e32 v123, v123, v123
	v_max_f32_e32 v122, v122, v122
	v_max_f32_e32 v122, v122, v123
	v_mov_b32_e32 v123, v122
	s_nop 1
	v_permlane32_swap_b32_e32 v122, v123
	v_max_f32_e32 v123, v123, v123
	v_max_f32_e32 v122, v122, v122
	v_max_f32_e32 v122, v122, v123
	v_mul_f32_e32 v138, 0xbfb8aa3b, v122
	v_fmamk_f32 v94, v94, 0x3fb8aa3b, v138
	v_exp_f32_e32 v94, v94
	v_fmamk_f32 v95, v95, 0x3fb8aa3b, v138
	v_exp_f32_e32 v95, v95
	v_fmamk_f32 v96, v96, 0x3fb8aa3b, v138
	v_exp_f32_e32 v96, v96
	v_fmamk_f32 v97, v97, 0x3fb8aa3b, v138
	v_exp_f32_e32 v97, v97
	v_add_f32_e32 v122, 0, v94
	v_add_f32_e32 v122, v95, v122
	v_add_f32_e32 v122, v96, v122
	v_add_f32_e32 v139, v97, v122
	v_fmamk_f32 v122, v130, 0x3fb8aa3b, v138
	v_exp_f32_e32 v122, v122
	v_fmamk_f32 v123, v131, 0x3fb8aa3b, v138
	v_exp_f32_e32 v123, v123
	v_fmamk_f32 v124, v132, 0x3fb8aa3b, v138
	v_exp_f32_e32 v124, v124
	v_fmamk_f32 v125, v133, 0x3fb8aa3b, v138
	v_exp_f32_e32 v125, v125
	v_add_f32_e32 v130, v122, v139
	v_add_f32_e32 v130, v123, v130
	v_add_f32_e32 v130, v124, v130
	v_add_f32_e32 v139, v125, v130
	v_fmamk_f32 v130, v134, 0x3fb8aa3b, v138
	v_exp_f32_e32 v130, v130
	v_fmamk_f32 v131, v135, 0x3fb8aa3b, v138
	v_exp_f32_e32 v131, v131
	v_fmamk_f32 v132, v136, 0x3fb8aa3b, v138
	v_exp_f32_e32 v132, v132
	v_fmamk_f32 v133, v137, 0x3fb8aa3b, v138
	v_exp_f32_e32 v133, v133
	v_fmamk_f32 v118, v118, 0x3fb8aa3b, v138
	v_add_f32_e32 v134, v130, v139
	v_exp_f32_e32 v118, v118
	v_fmamk_f32 v119, v119, 0x3fb8aa3b, v138
	v_add_f32_e32 v134, v131, v134
	v_exp_f32_e32 v119, v119
	v_fmamk_f32 v120, v120, 0x3fb8aa3b, v138
	v_add_f32_e32 v134, v132, v134
	v_exp_f32_e32 v120, v120
	v_fmac_f32_e32 v138, 0x3fb8aa3b, v121
	v_add_f32_e32 v134, v133, v134
	v_exp_f32_e32 v121, v138
	v_add_f32_e32 v134, v118, v134
	v_add_f32_e32 v134, v119, v134
	v_add_f32_e32 v134, v120, v134
	v_add_f32_e32 v134, v121, v134
	v_mov_b32_e32 v135, v134
	s_nop 1
	v_permlane16_swap_b32_e32 v134, v135
	v_add_f32_e32 v134, v134, v135
	v_mov_b32_e32 v135, v134
	s_nop 1
	v_permlane32_swap_b32_e32 v134, v135
	v_add_f32_e32 v134, v134, v135
	v_rcp_f32_e32 v134, v134
	v_lshl_add_u64 v[136:137], v[142:143], 4, s[20:21]
	global_store_dwordx4 v[136:137], v[90:93], off sc1
	s_nop 1
	v_pk_mul_f32 v[90:91], v[134:135], v[94:95] op_sel_hi:[0,1]
	v_pk_mul_f32 v[92:93], v[134:135], v[96:97] op_sel_hi:[0,1]
	v_cvt_pk_f16_f32 v90, v90, v91
	v_cvt_pk_f16_f32 v91, v92, v93
	v_lshl_add_u32 v94, v179, 3, v186
	ds_write_b64 v94, v[90:91]
	v_pk_mul_f32 v[90:91], v[134:135], v[122:123] op_sel_hi:[0,1]
	v_pk_mul_f32 v[92:93], v[134:135], v[124:125] op_sel_hi:[0,1]
	v_cvt_pk_f16_f32 v90, v90, v91
	v_cvt_pk_f16_f32 v91, v92, v93
	ds_write_b64 v94, v[90:91] offset:6464
	v_pk_mul_f32 v[90:91], v[134:135], v[130:131] op_sel_hi:[0,1]
	v_pk_mul_f32 v[92:93], v[134:135], v[132:133] op_sel_hi:[0,1]
	v_cvt_pk_f16_f32 v90, v90, v91
	v_cvt_pk_f16_f32 v91, v92, v93
	ds_write_b64 v94, v[90:91] offset:12928
	v_pk_mul_f32 v[90:91], v[134:135], v[118:119] op_sel_hi:[0,1]
	v_pk_mul_f32 v[92:93], v[134:135], v[120:121] op_sel_hi:[0,1]
	v_cvt_pk_f16_f32 v90, v90, v91
	v_cvt_pk_f16_f32 v91, v92, v93
	ds_write_b64 v94, v[90:91] offset:19392
	s_waitcnt lgkmcnt(0)
	s_and_saveexec_b64 s[8:9], s[14:15]
	s_lshl_b32 s10, s24, 2
	s_add_i32 s10, s10, 0x14a00
	v_mov_b32_e32 v90, 1
	v_mov_b32_e32 v91, s10
	ds_write_b32 v91, v90
	s_or_b64 exec, exec, s[8:9]
	s_waitcnt vmcnt(15)
	v_ashrrev_i32_e32 v179, 31, v178
	v_lshlrev_b64 v[90:91], 9, v[178:179]
	v_lshl_add_u64 v[90:91], s[12:13], 0, v[90:91]
	v_mov_b32_e32 v181, 0
	v_lshl_add_u64 v[178:179], v[90:91], 0, v[180:181]
	global_load_dwordx4 v[142:145], v[184:185], off offset:256
	global_load_dwordx4 v[138:141], v[184:185], off offset:320
	global_load_dwordx4 v[134:137], v[184:185], off offset:384
	global_load_dwordx4 v[130:133], v[184:185], off offset:448
	global_load_dwordx4 v[122:125], v[178:179], off
	global_load_dwordx4 v[118:121], v[178:179], off offset:64
	global_load_dwordx4 v[94:97], v[178:179], off offset:128
	global_load_dwordx4 v[90:93], v[178:179], off offset:192
	v_cvt_pk_f16_f32 v158, v158, v159
	v_cvt_pk_f16_f32 v159, v160, v161
	v_cvt_pk_f16_f32 v160, v154, v155
	v_cvt_pk_f16_f32 v161, v156, v157
	v_cvt_pk_f16_f32 v150, v150, v151
	v_cvt_pk_f16_f32 v151, v152, v153
	v_cvt_pk_f16_f32 v152, v146, v147
	v_cvt_pk_f16_f32 v153, v148, v149
	v_cvt_pk_f16_f32 v126, v126, v127
	v_cvt_pk_f16_f32 v127, v128, v129
	v_cvt_pk_f16_f32 v128, v114, v115
	v_cvt_pk_f16_f32 v129, v116, v117
	v_cvt_pk_f16_f32 v106, v106, v107
	v_cvt_pk_f16_f32 v107, v108, v109
	v_cvt_pk_f16_f32 v108, v98, v99
	v_cvt_pk_f16_f32 v109, v100, v101
	v_mov_b64_e32 v[98:99], v[158:159]
	s_and_b64 vcc, exec, s[6:7]
	v_mov_b64_e32 v[100:101], v[160:161]
	s_cbranch_vccnz .LBB0_63
	s_cmp_eq_u32 s33, 1
	s_cselect_b64 vcc, -1, 0
	s_cmp_eq_u32 s33, 2
	s_cselect_b64 s[8:9], -1, 0
	v_cndmask_b32_e64 v98, v106, v126, s[8:9]
	v_cndmask_b32_e64 v99, v107, v127, s[8:9]
	v_cndmask_b32_e64 v100, v108, v128, s[8:9]
	v_cndmask_b32_e64 v101, v109, v129, s[8:9]
	v_cndmask_b32_e32 v101, v101, v153, vcc
	v_cndmask_b32_e32 v100, v100, v152, vcc
	v_cndmask_b32_e32 v99, v99, v151, vcc
	v_cndmask_b32_e32 v98, v98, v150, vcc
.LBB0_63:
	v_mfma_f32_16x16x32_f16 v[114:117], v[30:33], v[158:161], 0
	s_add_i32 s8, s36, s40
	s_lshl_b32 s8, s8, 8
	s_or_b32 s8, s8, s38
	v_mfma_f32_16x16x32_f16 v[146:149], v[46:49], v[158:161], 0
	v_mfma_f32_16x16x32_f16 v[114:117], v[22:25], v[150:153], v[114:117]
	v_mfma_f32_16x16x32_f16 v[154:157], v[54:57], v[158:161], 0
	v_mfma_f32_16x16x32_f16 v[146:149], v[34:37], v[150:153], v[146:149]
	v_mfma_f32_16x16x32_f16 v[158:161], v[62:65], v[158:161], 0
	v_mfma_f32_16x16x32_f16 v[114:117], v[18:21], v[126:129], v[114:117]
	v_mfma_f32_16x16x32_f16 v[154:157], v[50:53], v[150:153], v[154:157]
	v_mfma_f32_16x16x32_f16 v[146:149], v[26:29], v[126:129], v[146:149]
	v_mfma_f32_16x16x32_f16 v[150:153], v[58:61], v[150:153], v[158:161]
	v_mfma_f32_16x16x32_f16 v[114:117], v[14:17], v[106:109], v[114:117]
	s_nop 2
	v_or_b32_e32 v158, s8, v1
	v_mfma_f32_16x16x32_f16 v[154:157], v[38:41], v[126:129], v[154:157]
	v_mfma_f32_16x16x32_f16 v[146:149], v[2:5], v[106:109], v[146:149]
	v_mfma_f32_16x16x32_f16 v[126:129], v[42:45], v[126:129], v[150:153]
	s_nop 2
	v_max_f32_e32 v150, v115, v115
	v_max_f32_e32 v151, v114, v114
	v_max_f32_e32 v150, v151, v150
	v_max3_f32 v150, v150, v116, v117
	v_max3_f32 v159, v150, v146, v147
	v_mfma_f32_16x16x32_f16 v[150:153], v[6:9], v[106:109], v[154:157]
	v_mfma_f32_16x16x32_f16 v[106:109], v[10:13], v[106:109], v[126:129]
	s_nop 1
	v_max3_f32 v154, v159, v148, v149
	s_nop 3
	v_max3_f32 v154, v154, v150, v151
	v_max3_f32 v154, v154, v152, v153
	v_ashrrev_i32_e32 v159, 31, v158
	v_max3_f32 v126, v154, v106, v107
	v_max3_f32 v126, v126, v108, v109
	v_mov_b32_e32 v127, v126
	s_nop 1
	v_permlane16_swap_b32_e32 v126, v127
	v_max_f32_e32 v127, v127, v127
	v_max_f32_e32 v126, v126, v126
	v_max_f32_e32 v126, v126, v127
	v_mov_b32_e32 v127, v126
	s_nop 1
	v_permlane32_swap_b32_e32 v126, v127
	v_max_f32_e32 v127, v127, v127
	v_max_f32_e32 v126, v126, v126
	v_max_f32_e32 v126, v126, v127
	v_mul_f32_e32 v154, 0xbfb8aa3b, v126
	v_fmamk_f32 v114, v114, 0x3fb8aa3b, v154
	v_exp_f32_e32 v114, v114
	v_fmamk_f32 v115, v115, 0x3fb8aa3b, v154
	v_exp_f32_e32 v115, v115
	v_fmamk_f32 v116, v116, 0x3fb8aa3b, v154
	v_exp_f32_e32 v116, v116
	v_fmamk_f32 v117, v117, 0x3fb8aa3b, v154
	v_exp_f32_e32 v117, v117
	v_add_f32_e32 v126, 0, v114
	v_add_f32_e32 v126, v115, v126
	v_add_f32_e32 v126, v116, v126
	v_add_f32_e32 v155, v117, v126
	v_fmamk_f32 v126, v146, 0x3fb8aa3b, v154
	v_exp_f32_e32 v126, v126
	v_fmamk_f32 v127, v147, 0x3fb8aa3b, v154
	v_exp_f32_e32 v127, v127
	v_fmamk_f32 v128, v148, 0x3fb8aa3b, v154
	v_exp_f32_e32 v128, v128
	v_fmamk_f32 v129, v149, 0x3fb8aa3b, v154
	v_exp_f32_e32 v129, v129
	v_add_f32_e32 v146, v126, v155
	v_add_f32_e32 v146, v127, v146
	v_add_f32_e32 v146, v128, v146
	v_add_f32_e32 v155, v129, v146
	v_fmamk_f32 v146, v150, 0x3fb8aa3b, v154
	v_exp_f32_e32 v146, v146
	v_fmamk_f32 v147, v151, 0x3fb8aa3b, v154
	v_exp_f32_e32 v147, v147
	v_fmamk_f32 v148, v152, 0x3fb8aa3b, v154
	v_exp_f32_e32 v148, v148
	v_fmamk_f32 v149, v153, 0x3fb8aa3b, v154
	v_exp_f32_e32 v149, v149
	v_fmamk_f32 v106, v106, 0x3fb8aa3b, v154
	v_add_f32_e32 v150, v146, v155
	v_exp_f32_e32 v106, v106
	v_fmamk_f32 v107, v107, 0x3fb8aa3b, v154
	v_add_f32_e32 v150, v147, v150
	v_exp_f32_e32 v107, v107
	v_fmamk_f32 v108, v108, 0x3fb8aa3b, v154
	v_add_f32_e32 v150, v148, v150
	v_exp_f32_e32 v108, v108
	v_fmac_f32_e32 v154, 0x3fb8aa3b, v109
	v_add_f32_e32 v150, v149, v150
	v_exp_f32_e32 v109, v154
	v_add_f32_e32 v150, v106, v150
	v_add_f32_e32 v150, v107, v150
	v_add_f32_e32 v150, v108, v150
	v_add_f32_e32 v150, v109, v150
	v_mov_b32_e32 v151, v150
	s_nop 1
	v_permlane16_swap_b32_e32 v150, v151
	v_add_f32_e32 v150, v150, v151
	v_mov_b32_e32 v151, v150
	s_nop 1
	v_permlane32_swap_b32_e32 v150, v151
	v_add_f32_e32 v150, v150, v151
	v_rcp_f32_e32 v150, v150
	v_lshl_add_u64 v[152:153], v[158:159], 4, s[20:21]
	global_store_dwordx4 v[152:153], v[98:101], off sc1
	s_nop 1
	v_pk_mul_f32 v[98:99], v[150:151], v[114:115] op_sel_hi:[0,1]
	v_pk_mul_f32 v[100:101], v[150:151], v[116:117] op_sel_hi:[0,1]
	v_cvt_pk_f16_f32 v98, v98, v99
	v_cvt_pk_f16_f32 v99, v100, v101
	v_lshl_add_u32 v114, v204, 3, v186
	ds_write_b64 v114, v[98:99]
	v_pk_mul_f32 v[98:99], v[150:151], v[126:127] op_sel_hi:[0,1]
	v_pk_mul_f32 v[100:101], v[150:151], v[128:129] op_sel_hi:[0,1]
	v_cvt_pk_f16_f32 v98, v98, v99
	v_cvt_pk_f16_f32 v99, v100, v101
	ds_write_b64 v114, v[98:99] offset:6464
	v_pk_mul_f32 v[98:99], v[150:151], v[146:147] op_sel_hi:[0,1]
	v_pk_mul_f32 v[100:101], v[150:151], v[148:149] op_sel_hi:[0,1]
	v_cvt_pk_f16_f32 v98, v98, v99
	v_cvt_pk_f16_f32 v99, v100, v101
	ds_write_b64 v114, v[98:99] offset:12928
	v_pk_mul_f32 v[98:99], v[150:151], v[106:107] op_sel_hi:[0,1]
	v_pk_mul_f32 v[100:101], v[150:151], v[108:109] op_sel_hi:[0,1]
	v_cvt_pk_f16_f32 v98, v98, v99
	v_cvt_pk_f16_f32 v99, v100, v101
	ds_write_b64 v114, v[98:99] offset:19392
	s_waitcnt lgkmcnt(0)
	s_and_saveexec_b64 s[8:9], s[14:15]
	s_lshl_b32 s10, s36, 2
	s_add_i32 s10, s10, 0x14a00
	v_mov_b32_e32 v98, 1
	v_mov_b32_e32 v99, s10
	ds_write_b32 v99, v98
	s_or_b64 exec, exec, s[8:9]
	global_load_dwordx4 v[158:161], v[178:179], off offset:256
	global_load_dwordx4 v[154:157], v[178:179], off offset:320
	global_load_dwordx4 v[150:153], v[178:179], off offset:384
	global_load_dwordx4 v[146:149], v[178:179], off offset:448
	v_mov_b32_e32 v181, 0
	s_waitcnt vmcnt(18)
	v_ashrrev_i32_e32 v183, 31, v182
	v_lshl_add_u64 v[98:99], s[12:13], 0, v[180:181]
	v_lshlrev_b64 v[100:101], 9, v[182:183]
	s_cmp_eq_u32 s42, 0
	v_lshl_add_u64 v[182:183], v[98:99], 0, v[100:101]
	s_cselect_b64 s[24:25], -1, 0
	s_cmp_lg_u32 s42, 0
	v_mov_b64_e32 v[98:99], v[174:175]
	v_mov_b64_e32 v[100:101], v[176:177]
	v_mov_b64_e32 v[106:107], v[170:171]
	v_mov_b64_e32 v[108:109], v[172:173]
	v_mov_b64_e32 v[114:115], v[166:167]
	v_mov_b64_e32 v[116:117], v[168:169]
	v_mov_b64_e32 v[126:127], v[162:163]
	v_mov_b64_e32 v[128:129], v[164:165]
	s_cbranch_scc1 .LBB0_67
	global_load_dwordx4 v[98:101], v[182:183], off
	global_load_dwordx4 v[106:109], v[182:183], off offset:64
	global_load_dwordx4 v[114:117], v[182:183], off offset:128
	global_load_dwordx4 v[126:129], v[182:183], off offset:192

.LBB0_69:
	v_mfma_f32_16x16x32_f16 v[188:191], v[30:33], v[174:177], 0
	s_add_i32 s12, s39, s40
	v_lshl_or_b32 v184, s12, 8, v1
	s_movk_i32 s12, 0xc8
	v_mfma_f32_16x16x32_f16 v[192:195], v[46:49], v[174:177], 0
	v_mfma_f32_16x16x32_f16 v[200:203], v[54:57], v[174:177], 0
	v_mfma_f32_16x16x32_f16 v[174:177], v[62:65], v[174:177], 0
	v_mfma_f32_16x16x32_f16 v[188:191], v[22:25], v[166:169], v[188:191]
	v_mfma_f32_16x16x32_f16 v[192:195], v[34:37], v[166:169], v[192:195]
	v_mfma_f32_16x16x32_f16 v[200:203], v[50:53], v[166:169], v[200:203]
	v_mfma_f32_16x16x32_f16 v[166:169], v[58:61], v[166:169], v[174:177]
	v_mfma_f32_16x16x32_f16 v[174:177], v[18:21], v[170:173], v[188:191]
	v_mfma_f32_16x16x32_f16 v[188:191], v[26:29], v[170:173], v[192:195]
	v_mfma_f32_16x16x32_f16 v[192:195], v[38:41], v[170:173], v[200:203]
	v_mfma_f32_16x16x32_f16 v[166:169], v[42:45], v[170:173], v[166:169]
	v_or_b32_e32 v170, s38, v184
	v_ashrrev_i32_e32 v171, 31, v170
	v_lshl_add_u64 v[184:185], v[170:171], 4, s[20:21]
	v_mfma_f32_16x16x32_f16 v[170:173], v[14:17], v[162:165], v[174:177]
	global_store_dwordx4 v[184:185], v[178:181], off sc1
	v_mfma_f32_16x16x32_f16 v[174:177], v[2:5], v[162:165], v[188:191]
	v_mfma_f32_16x16x32_f16 v[188:191], v[10:13], v[162:165], v[166:169]
	s_nop 4
	v_max_f32_e32 v178, v171, v171
	v_max_f32_e32 v179, v170, v170
	v_max_f32_e32 v178, v179, v178
	v_max3_f32 v178, v178, v172, v173
	v_max3_f32 v184, v178, v174, v175
	v_mfma_f32_16x16x32_f16 v[178:181], v[6:9], v[162:165], v[192:195]
	v_max3_f32 v184, v184, v176, v177
	s_nop 6
	v_max3_f32 v184, v184, v178, v179
	v_max3_f32 v184, v184, v180, v181
	v_max3_f32 v162, v184, v188, v189
	v_max3_f32 v162, v162, v190, v191
	v_mov_b32_e32 v163, v162
	s_nop 1
	v_permlane16_swap_b32_e32 v162, v163
	v_max_f32_e32 v163, v163, v163
	v_max_f32_e32 v162, v162, v162
	v_max_f32_e32 v162, v162, v163
	v_mov_b32_e32 v163, v162
	s_nop 1
	v_permlane32_swap_b32_e32 v162, v163
	v_max_f32_e32 v163, v163, v163
	v_max_f32_e32 v162, v162, v162
	v_max_f32_e32 v162, v162, v163
	v_mul_f32_e32 v184, 0xbfb8aa3b, v162
	v_fmamk_f32 v162, v170, 0x3fb8aa3b, v184
	v_exp_f32_e32 v162, v162
	v_fmamk_f32 v163, v171, 0x3fb8aa3b, v184
	v_exp_f32_e32 v163, v163
	v_fmamk_f32 v164, v172, 0x3fb8aa3b, v184
	v_exp_f32_e32 v164, v164
	v_fmamk_f32 v165, v173, 0x3fb8aa3b, v184
	v_exp_f32_e32 v165, v165
	v_add_f32_e32 v166, 0, v162
	v_add_f32_e32 v166, v163, v166
	v_add_f32_e32 v166, v164, v166
	v_add_f32_e32 v170, v165, v166
	v_fmamk_f32 v166, v174, 0x3fb8aa3b, v184
	v_exp_f32_e32 v166, v166
	v_fmamk_f32 v167, v175, 0x3fb8aa3b, v184
	v_exp_f32_e32 v167, v167
	v_fmamk_f32 v168, v176, 0x3fb8aa3b, v184
	v_exp_f32_e32 v168, v168
	v_fmamk_f32 v169, v177, 0x3fb8aa3b, v184
	v_exp_f32_e32 v169, v169
	v_add_f32_e32 v170, v166, v170
	v_add_f32_e32 v170, v167, v170
	v_add_f32_e32 v170, v168, v170
	v_add_f32_e32 v174, v169, v170
	v_fmamk_f32 v170, v178, 0x3fb8aa3b, v184
	v_exp_f32_e32 v170, v170
	v_fmamk_f32 v171, v179, 0x3fb8aa3b, v184
	v_exp_f32_e32 v171, v171
	v_fmamk_f32 v172, v180, 0x3fb8aa3b, v184
	v_exp_f32_e32 v172, v172
	v_fmamk_f32 v173, v181, 0x3fb8aa3b, v184
	v_exp_f32_e32 v173, v173
	v_add_f32_e32 v174, v170, v174
	v_add_f32_e32 v174, v171, v174
	v_add_f32_e32 v174, v172, v174
	v_add_f32_e32 v178, v173, v174
	v_fmamk_f32 v174, v188, 0x3fb8aa3b, v184
	v_exp_f32_e32 v174, v174
	v_fmamk_f32 v175, v189, 0x3fb8aa3b, v184
	v_exp_f32_e32 v175, v175
	v_fmamk_f32 v176, v190, 0x3fb8aa3b, v184
	v_exp_f32_e32 v176, v176
	v_fmac_f32_e32 v184, 0x3fb8aa3b, v191
	v_exp_f32_e32 v177, v184
	v_add_f32_e32 v178, v174, v178
	v_add_f32_e32 v178, v175, v178
	v_add_f32_e32 v178, v176, v178
	v_add_f32_e32 v179, v177, v178
	v_mov_b32_e32 v180, v179
	s_nop 1
	v_permlane16_swap_b32_e32 v179, v180
	v_add_f32_e32 v179, v179, v180
	v_or_b32_e32 v178, s41, v199
	v_mov_b32_e32 v180, v179
	s_nop 1
	v_permlane32_swap_b32_e32 v179, v180
	v_cmp_gt_u32_e32 vcc, s12, v178
	s_and_saveexec_b64 s[12:13], vcc
	s_cbranch_execz .LBB0_71
	v_add_f32_e32 v179, v179, v180
	v_rcp_f32_e32 v180, v179
	v_lshl_add_u32 v178, v178, 3, v186
	v_pk_mul_f32 v[162:163], v[180:181], v[162:163] op_sel_hi:[0,1]
	v_pk_mul_f32 v[164:165], v[180:181], v[164:165] op_sel_hi:[0,1]
	v_cvt_pk_f16_f32 v162, v162, v163
	v_cvt_pk_f16_f32 v163, v164, v165
	ds_write_b64 v178, v[162:163]
	v_pk_mul_f32 v[162:163], v[180:181], v[166:167] op_sel_hi:[0,1]
	v_pk_mul_f32 v[164:165], v[180:181], v[168:169] op_sel_hi:[0,1]
	v_cvt_pk_f16_f32 v162, v162, v163
	v_cvt_pk_f16_f32 v163, v164, v165
	ds_write_b64 v178, v[162:163] offset:6464
	v_pk_mul_f32 v[162:163], v[180:181], v[170:171] op_sel_hi:[0,1]
	v_pk_mul_f32 v[164:165], v[180:181], v[172:173] op_sel_hi:[0,1]
	v_cvt_pk_f16_f32 v162, v162, v163
	v_cvt_pk_f16_f32 v163, v164, v165
	ds_write_b64 v178, v[162:163] offset:12928
	v_pk_mul_f32 v[162:163], v[180:181], v[174:175] op_sel_hi:[0,1]
	v_pk_mul_f32 v[164:165], v[180:181], v[176:177] op_sel_hi:[0,1]
	v_cvt_pk_f16_f32 v162, v162, v163
	v_cvt_pk_f16_f32 v163, v164, v165
	ds_write_b64 v178, v[162:163] offset:19392

.Lc0_dback0:
	v_pk_add_f16 v112, v112, v116
	v_pk_add_f16 v113, v113, v117
	v_pk_add_f16 v114, v114, v118
	v_pk_add_f16 v115, v115, v119
	global_store_dwordx4 v35, v[112:115], s[68:69] offset:-1024 sc1

.Lc0_dback1:
	v_pk_add_f16 v112, v112, v116
	v_pk_add_f16 v113, v113, v117
	v_pk_add_f16 v114, v114, v118
	v_pk_add_f16 v115, v115, v119
	global_store_dwordx4 v35, v[112:115], s[68:69] offset:0 sc1

.Lc0_fin2:
	ds_read_b128 v[112:115], v43 offset:2048
	ds_read_b128 v[116:119], v43 offset:3072
	s_waitcnt lgkmcnt(0)
	v_pk_add_f16 v112, v112, v116
	v_pk_add_f16 v113, v113, v117
	v_pk_add_f16 v114, v114, v118
	v_pk_add_f16 v115, v115, v119
	s_mov_b32 exec_lo, -1
	s_mov_b32 exec_hi, 0
	global_store_dwordx4 v35, v[112:115], s[68:69] sc1

.LBB0_108:
	s_waitcnt vmcnt(18)
	v_cvt_pk_f16_f32 v110, v110, v111
	v_cvt_pk_f16_f32 v111, v112, v113
	s_waitcnt vmcnt(17)
	v_cvt_pk_f16_f32 v112, v102, v103
	v_cvt_pk_f16_f32 v113, v104, v105
	s_waitcnt vmcnt(16)
	v_cvt_pk_f16_f32 v86, v86, v87
	v_cvt_pk_f16_f32 v87, v88, v89
	v_mfma_f32_16x16x32_f16 v[102:105], v[30:33], v[110:113], 0
	s_waitcnt vmcnt(15)
	v_cvt_pk_f16_f32 v88, v82, v83
	v_cvt_pk_f16_f32 v89, v84, v85
	s_waitcnt vmcnt(13)
	v_cvt_pk_f16_f32 v82, v142, v143
	v_mfma_f32_16x16x32_f16 v[162:165], v[46:49], v[110:113], 0
	v_cvt_pk_f16_f32 v83, v144, v145
	s_waitcnt vmcnt(12)
	v_cvt_pk_f16_f32 v84, v138, v139
	v_cvt_pk_f16_f32 v85, v140, v141
	v_mfma_f32_16x16x32_f16 v[166:169], v[54:57], v[110:113], 0
	s_waitcnt vmcnt(11)
	v_cvt_pk_f16_f32 v134, v134, v135
	v_cvt_pk_f16_f32 v135, v136, v137
	s_waitcnt vmcnt(10)
	v_cvt_pk_f16_f32 v136, v130, v131
	v_mfma_f32_16x16x32_f16 v[102:105], v[22:25], v[86:89], v[102:105]
	v_cvt_pk_f16_f32 v137, v132, v133
	s_add_i32 s24, s36, 4
	s_add_i32 s25, s24, s40
	v_mfma_f32_16x16x32_f16 v[170:173], v[62:65], v[110:113], 0
	v_mfma_f32_16x16x32_f16 v[138:141], v[34:37], v[86:89], v[162:165]
	v_mfma_f32_16x16x32_f16 v[142:145], v[50:53], v[86:89], v[166:169]
	s_nop 1
	v_cndmask_b32_e64 v162, v137, v85, s[10:11]
	v_cndmask_b32_e64 v163, v136, v84, s[10:11]
	v_cndmask_b32_e64 v164, v135, v83, s[10:11]
	v_mfma_f32_16x16x32_f16 v[102:105], v[18:21], v[82:85], v[102:105]
	v_cndmask_b32_e64 v165, v134, v82, s[10:11]
	v_cndmask_b32_e64 v165, v165, v86, s[8:9]
	v_cndmask_b32_e64 v164, v164, v87, s[8:9]
	v_mfma_f32_16x16x32_f16 v[130:133], v[58:61], v[86:89], v[170:173]
	v_cndmask_b32_e64 v163, v163, v88, s[8:9]
	v_cndmask_b32_e64 v162, v162, v89, s[8:9]
	v_cndmask_b32_e64 v113, v162, v113, s[4:5]
	v_mfma_f32_16x16x32_f16 v[86:89], v[26:29], v[82:85], v[138:141]
	v_cndmask_b32_e64 v112, v163, v112, s[4:5]
	v_cndmask_b32_e64 v111, v164, v111, s[4:5]
	v_cndmask_b32_e64 v110, v165, v110, s[4:5]
	v_mfma_f32_16x16x32_f16 v[138:141], v[38:41], v[82:85], v[142:145]
	s_nop 2
	v_lshl_or_b32 v142, s25, 8, v1
	v_mfma_f32_16x16x32_f16 v[102:105], v[14:17], v[134:137], v[102:105]
	v_mfma_f32_16x16x32_f16 v[82:85], v[42:45], v[82:85], v[130:133]
	s_nop 2
	v_or_b32_e32 v130, s38, v142
	v_ashrrev_i32_e32 v131, 31, v130
	v_lshl_add_u64 v[130:131], v[130:131], 4, s[20:21]
	v_mfma_f32_16x16x32_f16 v[86:89], v[2:5], v[134:137], v[86:89]
	global_store_dwordx4 v[130:131], v[110:113], off sc1
	s_nop 1
	v_max_f32_e32 v110, v103, v103
	v_max_f32_e32 v111, v102, v102
	v_max_f32_e32 v110, v111, v110
	v_max3_f32 v110, v110, v104, v105
	s_nop 0
	v_max3_f32 v130, v110, v86, v87
	v_mfma_f32_16x16x32_f16 v[110:113], v[6:9], v[134:137], v[138:141]
	v_max3_f32 v130, v130, v88, v89
	s_nop 6
	v_max3_f32 v130, v130, v110, v111
	v_max3_f32 v138, v130, v112, v113
	v_mfma_f32_16x16x32_f16 v[130:133], v[10:13], v[134:137], v[82:85]
	s_nop 7
	v_max3_f32 v82, v138, v130, v131
	v_max3_f32 v82, v82, v132, v133
	v_mov_b32_e32 v83, v82
	s_nop 1
	v_permlane16_swap_b32_e32 v82, v83
	v_max_f32_e32 v83, v83, v83
	v_max_f32_e32 v82, v82, v82
	v_max_f32_e32 v82, v82, v83
	v_mov_b32_e32 v83, v82
	s_nop 1
	v_permlane32_swap_b32_e32 v82, v83
	v_max_f32_e32 v83, v83, v83
	v_max_f32_e32 v82, v82, v82
	v_max_f32_e32 v82, v82, v83
	v_mul_f32_e32 v134, 0xbfb8aa3b, v82
	v_fmamk_f32 v82, v102, 0x3fb8aa3b, v134
	v_exp_f32_e32 v82, v82
	v_fmamk_f32 v83, v103, 0x3fb8aa3b, v134
	v_exp_f32_e32 v83, v83
	v_fmamk_f32 v84, v104, 0x3fb8aa3b, v134
	v_exp_f32_e32 v84, v84
	v_fmamk_f32 v85, v105, 0x3fb8aa3b, v134
	v_exp_f32_e32 v85, v85
	v_fmamk_f32 v86, v86, 0x3fb8aa3b, v134
	v_add_f32_e32 v102, 0, v82
	v_exp_f32_e32 v86, v86
	v_fmamk_f32 v87, v87, 0x3fb8aa3b, v134
	v_add_f32_e32 v102, v83, v102
	v_exp_f32_e32 v87, v87
	v_fmamk_f32 v88, v88, 0x3fb8aa3b, v134
	v_add_f32_e32 v102, v84, v102
	v_exp_f32_e32 v88, v88
	v_fmamk_f32 v89, v89, 0x3fb8aa3b, v134
	v_add_f32_e32 v102, v85, v102
	v_exp_f32_e32 v89, v89
	v_add_f32_e32 v102, v86, v102
	v_add_f32_e32 v102, v87, v102
	v_add_f32_e32 v102, v88, v102
	v_add_f32_e32 v135, v89, v102
	v_fmamk_f32 v102, v110, 0x3fb8aa3b, v134
	v_exp_f32_e32 v102, v102
	v_fmamk_f32 v103, v111, 0x3fb8aa3b, v134
	v_exp_f32_e32 v103, v103
	v_fmamk_f32 v104, v112, 0x3fb8aa3b, v134
	v_exp_f32_e32 v104, v104
	v_fmamk_f32 v105, v113, 0x3fb8aa3b, v134
	v_exp_f32_e32 v105, v105
	v_add_f32_e32 v110, v102, v135
	v_add_f32_e32 v110, v103, v110
	v_add_f32_e32 v110, v104, v110
	v_add_f32_e32 v135, v105, v110
	v_fmamk_f32 v110, v130, 0x3fb8aa3b, v134
	v_exp_f32_e32 v110, v110
	v_fmamk_f32 v111, v131, 0x3fb8aa3b, v134
	v_exp_f32_e32 v111, v111
	v_fmamk_f32 v112, v132, 0x3fb8aa3b, v134
	v_exp_f32_e32 v112, v112
	v_fmac_f32_e32 v134, 0x3fb8aa3b, v133
	v_exp_f32_e32 v113, v134
	v_add_f32_e32 v130, v110, v135
	v_add_f32_e32 v130, v111, v130
	v_add_f32_e32 v130, v112, v130
	v_add_f32_e32 v131, v113, v130
	v_mov_b32_e32 v132, v131
	s_nop 1
	v_permlane16_swap_b32_e32 v131, v132
	v_add_f32_e32 v131, v131, v132
	v_lshl_or_b32 v130, s24, 4, v199
	v_mov_b32_e32 v132, v131
	s_movk_i32 s24, 0xc8
	s_nop 0
	v_permlane32_swap_b32_e32 v131, v132
	v_cmp_gt_u32_e32 vcc, s24, v130
	s_and_saveexec_b64 s[24:25], vcc
	s_cbranch_execz .LBB0_110
	v_add_f32_e32 v131, v131, v132
	v_rcp_f32_e32 v132, v131
	v_lshl_add_u32 v130, v130, 3, v186
	v_pk_mul_f32 v[82:83], v[132:133], v[82:83] op_sel_hi:[0,1]
	v_pk_mul_f32 v[84:85], v[132:133], v[84:85] op_sel_hi:[0,1]
	v_cvt_pk_f16_f32 v82, v82, v83
	v_cvt_pk_f16_f32 v83, v84, v85
	ds_write_b64 v130, v[82:83]
	v_pk_mul_f32 v[82:83], v[132:133], v[86:87] op_sel_hi:[0,1]
	v_pk_mul_f32 v[84:85], v[132:133], v[88:89] op_sel_hi:[0,1]
	v_cvt_pk_f16_f32 v82, v82, v83
	v_cvt_pk_f16_f32 v83, v84, v85
	ds_write_b64 v130, v[82:83] offset:6464
	v_pk_mul_f32 v[82:83], v[132:133], v[102:103] op_sel_hi:[0,1]
	v_pk_mul_f32 v[84:85], v[132:133], v[104:105] op_sel_hi:[0,1]
	v_cvt_pk_f16_f32 v82, v82, v83
	v_cvt_pk_f16_f32 v83, v84, v85
	ds_write_b64 v130, v[82:83] offset:12928
	v_pk_mul_f32 v[82:83], v[132:133], v[110:111] op_sel_hi:[0,1]
	v_pk_mul_f32 v[84:85], v[132:133], v[112:113] op_sel_hi:[0,1]
	v_cvt_pk_f16_f32 v82, v82, v83
	v_cvt_pk_f16_f32 v83, v84, v85
	ds_write_b64 v130, v[82:83] offset:19392

.LBB0_113:
	s_waitcnt vmcnt(9)
	v_cvt_pk_f16_f32 v82, v122, v123
	v_cvt_pk_f16_f32 v83, v124, v125
	s_waitcnt vmcnt(8)
	v_cvt_pk_f16_f32 v84, v118, v119
	v_cvt_pk_f16_f32 v85, v120, v121
	s_waitcnt vmcnt(7)
	v_cvt_pk_f16_f32 v94, v94, v95
	v_cvt_pk_f16_f32 v95, v96, v97
	v_mfma_f32_16x16x32_f16 v[86:89], v[30:33], v[82:85], 0
	s_waitcnt vmcnt(6)
	v_cvt_pk_f16_f32 v96, v90, v91
	v_cvt_pk_f16_f32 v97, v92, v93
	s_waitcnt vmcnt(4)
	v_cvt_pk_f16_f32 v90, v158, v159
	v_mfma_f32_16x16x32_f16 v[102:105], v[46:49], v[82:85], 0
	v_cvt_pk_f16_f32 v91, v160, v161
	s_waitcnt vmcnt(3)
	v_cvt_pk_f16_f32 v92, v154, v155
	v_cvt_pk_f16_f32 v93, v156, v157
	v_mfma_f32_16x16x32_f16 v[110:113], v[54:57], v[82:85], 0
	s_waitcnt vmcnt(2)
	v_cvt_pk_f16_f32 v122, v150, v151
	v_cvt_pk_f16_f32 v123, v152, v153
	s_waitcnt vmcnt(1)
	v_cvt_pk_f16_f32 v124, v146, v147
	v_mfma_f32_16x16x32_f16 v[86:89], v[22:25], v[94:97], v[86:89]
	v_cvt_pk_f16_f32 v125, v148, v149
	v_cndmask_b32_e64 v130, v125, v93, s[10:11]
	v_cndmask_b32_e64 v131, v124, v92, s[10:11]
	v_mfma_f32_16x16x32_f16 v[118:121], v[62:65], v[82:85], 0
	v_cndmask_b32_e64 v132, v123, v91, s[10:11]
	v_cndmask_b32_e64 v133, v122, v90, s[10:11]
	s_add_i32 s24, s36, 6
	v_mfma_f32_16x16x32_f16 v[102:105], v[34:37], v[94:97], v[102:105]
	v_cndmask_b32_e64 v133, v133, v94, s[8:9]
	v_cndmask_b32_e64 v132, v132, v95, s[8:9]
	v_cndmask_b32_e64 v131, v131, v96, s[8:9]
	v_mfma_f32_16x16x32_f16 v[110:113], v[50:53], v[94:97], v[110:113]
	v_cndmask_b32_e64 v130, v130, v97, s[8:9]
	v_cndmask_b32_e64 v85, v130, v85, s[4:5]
	v_cndmask_b32_e64 v84, v131, v84, s[4:5]
	v_mfma_f32_16x16x32_f16 v[86:89], v[18:21], v[90:93], v[86:89]
	v_cndmask_b32_e64 v83, v132, v83, s[4:5]
	v_cndmask_b32_e64 v82, v133, v82, s[4:5]
	s_add_i32 s4, s24, s40
	v_mfma_f32_16x16x32_f16 v[118:121], v[58:61], v[94:97], v[118:121]
	v_mfma_f32_16x16x32_f16 v[94:97], v[26:29], v[90:93], v[102:105]
	v_mfma_f32_16x16x32_f16 v[102:105], v[38:41], v[90:93], v[110:113]
	s_nop 2
	v_lshl_or_b32 v110, s4, 8, v1
	v_mfma_f32_16x16x32_f16 v[86:89], v[14:17], v[122:125], v[86:89]
	v_or_b32_e32 v110, s38, v110
	v_ashrrev_i32_e32 v111, 31, v110
	v_lshl_add_u64 v[110:111], v[110:111], 4, s[20:21]
	v_mfma_f32_16x16x32_f16 v[90:93], v[42:45], v[90:93], v[118:121]
	global_store_dwordx4 v[110:111], v[82:85], off sc1
	s_movk_i32 s4, 0xc8
	v_mfma_f32_16x16x32_f16 v[94:97], v[2:5], v[122:125], v[94:97]
	s_nop 0
	v_max_f32_e32 v82, v87, v87
	v_max_f32_e32 v83, v86, v86
	v_max_f32_e32 v82, v83, v82
	v_mfma_f32_16x16x32_f16 v[102:105], v[6:9], v[122:125], v[102:105]
	v_max3_f32 v82, v82, v88, v89
	s_nop 1
	v_max3_f32 v82, v82, v94, v95
	v_max3_f32 v82, v82, v96, v97
	v_mfma_f32_16x16x32_f16 v[110:113], v[10:13], v[122:125], v[90:93]
	s_nop 1
	v_max3_f32 v82, v82, v102, v103
	v_max3_f32 v82, v82, v104, v105
	s_nop 3
	v_max3_f32 v82, v82, v110, v111
	v_max3_f32 v82, v82, v112, v113
	v_mov_b32_e32 v83, v82
	s_nop 1
	v_permlane16_swap_b32_e32 v82, v83
	v_max_f32_e32 v83, v83, v83
	v_max_f32_e32 v82, v82, v82
	v_max_f32_e32 v82, v82, v83
	v_mov_b32_e32 v83, v82
	s_nop 1
	v_permlane32_swap_b32_e32 v82, v83
	v_max_f32_e32 v83, v83, v83
	v_max_f32_e32 v82, v82, v82
	v_max_f32_e32 v82, v82, v83
	v_mul_f32_e32 v118, 0xbfb8aa3b, v82
	v_fmamk_f32 v82, v86, 0x3fb8aa3b, v118
	v_exp_f32_e32 v82, v82
	v_fmamk_f32 v83, v87, 0x3fb8aa3b, v118
	v_exp_f32_e32 v83, v83
	v_fmamk_f32 v84, v88, 0x3fb8aa3b, v118
	v_exp_f32_e32 v84, v84
	v_fmamk_f32 v85, v89, 0x3fb8aa3b, v118
	v_exp_f32_e32 v85, v85
	v_add_f32_e32 v86, 0, v82
	v_add_f32_e32 v86, v83, v86
	v_add_f32_e32 v86, v84, v86
	v_add_f32_e32 v90, v85, v86
	v_fmamk_f32 v86, v94, 0x3fb8aa3b, v118
	v_exp_f32_e32 v86, v86
	v_fmamk_f32 v87, v95, 0x3fb8aa3b, v118
	v_exp_f32_e32 v87, v87
	v_fmamk_f32 v88, v96, 0x3fb8aa3b, v118
	v_exp_f32_e32 v88, v88
	v_fmamk_f32 v89, v97, 0x3fb8aa3b, v118
	v_exp_f32_e32 v89, v89
	v_add_f32_e32 v90, v86, v90
	v_add_f32_e32 v90, v87, v90
	v_add_f32_e32 v90, v88, v90
	v_add_f32_e32 v94, v89, v90
	v_fmamk_f32 v90, v102, 0x3fb8aa3b, v118
	v_exp_f32_e32 v90, v90
	v_fmamk_f32 v91, v103, 0x3fb8aa3b, v118
	v_exp_f32_e32 v91, v91
	v_fmamk_f32 v92, v104, 0x3fb8aa3b, v118
	v_exp_f32_e32 v92, v92
	v_fmamk_f32 v93, v105, 0x3fb8aa3b, v118
	v_exp_f32_e32 v93, v93
	v_add_f32_e32 v94, v90, v94
	v_add_f32_e32 v94, v91, v94
	v_add_f32_e32 v94, v92, v94
	v_add_f32_e32 v102, v93, v94
	v_fmamk_f32 v94, v110, 0x3fb8aa3b, v118
	v_exp_f32_e32 v94, v94
	v_fmamk_f32 v95, v111, 0x3fb8aa3b, v118
	v_exp_f32_e32 v95, v95
	v_fmamk_f32 v96, v112, 0x3fb8aa3b, v118
	v_exp_f32_e32 v96, v96
	v_fmac_f32_e32 v118, 0x3fb8aa3b, v113
	v_exp_f32_e32 v97, v118
	v_add_f32_e32 v102, v94, v102
	v_add_f32_e32 v102, v95, v102
	v_add_f32_e32 v102, v96, v102
	v_add_f32_e32 v103, v97, v102
	v_mov_b32_e32 v104, v103
	s_nop 1
	v_permlane16_swap_b32_e32 v103, v104
	v_add_f32_e32 v103, v103, v104
	v_lshl_or_b32 v102, s24, 4, v199
	v_mov_b32_e32 v104, v103
	s_nop 1
	v_permlane32_swap_b32_e32 v103, v104
	v_cmp_gt_u32_e32 vcc, s4, v102
	s_and_saveexec_b64 s[4:5], vcc
	s_cbranch_execz .LBB0_115
	v_add_f32_e32 v103, v103, v104
	v_rcp_f32_e32 v104, v103
	v_lshl_add_u32 v102, v102, 3, v186
	v_pk_mul_f32 v[82:83], v[104:105], v[82:83] op_sel_hi:[0,1]
	v_pk_mul_f32 v[84:85], v[104:105], v[84:85] op_sel_hi:[0,1]
	v_cvt_pk_f16_f32 v82, v82, v83
	v_cvt_pk_f16_f32 v83, v84, v85
	ds_write_b64 v102, v[82:83]
	v_pk_mul_f32 v[82:83], v[104:105], v[86:87] op_sel_hi:[0,1]
	v_pk_mul_f32 v[84:85], v[104:105], v[88:89] op_sel_hi:[0,1]
	v_cvt_pk_f16_f32 v82, v82, v83
	v_cvt_pk_f16_f32 v83, v84, v85
	ds_write_b64 v102, v[82:83] offset:6464
	v_pk_mul_f32 v[82:83], v[104:105], v[90:91] op_sel_hi:[0,1]
	v_pk_mul_f32 v[84:85], v[104:105], v[92:93] op_sel_hi:[0,1]
	v_cvt_pk_f16_f32 v82, v82, v83
	v_cvt_pk_f16_f32 v83, v84, v85
	ds_write_b64 v102, v[82:83] offset:12928
	v_pk_mul_f32 v[82:83], v[104:105], v[94:95] op_sel_hi:[0,1]
	v_pk_mul_f32 v[84:85], v[104:105], v[96:97] op_sel_hi:[0,1]
	v_cvt_pk_f16_f32 v82, v82, v83
	v_cvt_pk_f16_f32 v83, v84, v85
	ds_write_b64 v102, v[82:83] offset:19392

.LBB0_120:
	v_mfma_f32_16x16x32_f16 v[30:33], v[30:33], v[82:85], 0
	s_mul_i32 s4, s3, 0xd00
	s_addk_i32 s4, 0xc00
	v_mfma_f32_16x16x32_f16 v[46:49], v[46:49], v[82:85], 0
	v_mfma_f32_16x16x32_f16 v[54:57], v[54:57], v[82:85], 0
	v_mfma_f32_16x16x32_f16 v[22:25], v[22:25], v[86:89], v[30:33]
	v_mfma_f32_16x16x32_f16 v[62:65], v[62:65], v[82:85], 0
	v_mfma_f32_16x16x32_f16 v[30:33], v[34:37], v[86:89], v[46:49]
	v_mfma_f32_16x16x32_f16 v[34:37], v[50:53], v[86:89], v[54:57]
	v_mfma_f32_16x16x32_f16 v[18:21], v[18:21], v[90:93], v[22:25]
	v_mfma_f32_16x16x32_f16 v[46:49], v[58:61], v[86:89], v[62:65]
	v_mfma_f32_16x16x32_f16 v[22:25], v[26:29], v[90:93], v[30:33]
	v_mfma_f32_16x16x32_f16 v[26:29], v[38:41], v[90:93], v[34:37]
	s_nop 3
	v_or_b32_e32 v34, s4, v1
	v_mfma_f32_16x16x32_f16 v[14:17], v[14:17], v[66:69], v[18:21]
	v_or_b32_e32 v34, s38, v34
	v_ashrrev_i32_e32 v35, 31, v34
	v_lshl_add_u64 v[34:35], v[34:35], 4, s[20:21]
	v_mfma_f32_16x16x32_f16 v[30:33], v[42:45], v[90:93], v[46:49]
	global_store_dwordx4 v[34:35], v[70:73], off sc1
	s_nop 2
	v_max_f32_e32 v34, v15, v15
	v_max_f32_e32 v35, v14, v14
	v_mfma_f32_16x16x32_f16 v[18:21], v[2:5], v[66:69], v[22:25]
	v_max_f32_e32 v2, v35, v34
	v_max3_f32 v2, v2, v16, v17
	s_movk_i32 s4, 0xc8
	v_mfma_f32_16x16x32_f16 v[22:25], v[6:9], v[66:69], v[26:29]
	v_mfma_f32_16x16x32_f16 v[26:29], v[10:13], v[66:69], v[30:33]
	s_nop 2
	v_max3_f32 v2, v2, v18, v19
	v_max3_f32 v2, v2, v20, v21
	s_nop 1
	v_max3_f32 v2, v2, v22, v23
	v_max3_f32 v2, v2, v24, v25
	v_max3_f32 v2, v2, v26, v27
	v_max3_f32 v2, v2, v28, v29
	v_mov_b32_e32 v3, v2
	s_nop 1
	v_permlane16_swap_b32_e32 v2, v3
	v_max_f32_e32 v3, v3, v3
	v_max_f32_e32 v2, v2, v2
	v_max_f32_e32 v2, v2, v3
	v_mov_b32_e32 v3, v2
	s_nop 1
	v_permlane32_swap_b32_e32 v2, v3
	v_max_f32_e32 v3, v3, v3
	v_max_f32_e32 v2, v2, v2
	v_max_f32_e32 v2, v2, v3
	v_mul_f32_e32 v30, 0xbfb8aa3b, v2
	v_fmamk_f32 v2, v14, 0x3fb8aa3b, v30
	v_exp_f32_e32 v2, v2
	v_fmamk_f32 v3, v15, 0x3fb8aa3b, v30
	v_exp_f32_e32 v3, v3
	v_fmamk_f32 v4, v16, 0x3fb8aa3b, v30
	v_exp_f32_e32 v4, v4
	v_fmamk_f32 v5, v17, 0x3fb8aa3b, v30
	v_exp_f32_e32 v5, v5
	v_add_f32_e32 v6, 0, v2
	v_add_f32_e32 v6, v3, v6
	v_add_f32_e32 v6, v4, v6
	v_add_f32_e32 v10, v5, v6
	v_fmamk_f32 v6, v18, 0x3fb8aa3b, v30
	v_exp_f32_e32 v6, v6
	v_fmamk_f32 v7, v19, 0x3fb8aa3b, v30
	v_exp_f32_e32 v7, v7
	v_fmamk_f32 v8, v20, 0x3fb8aa3b, v30
	v_exp_f32_e32 v8, v8
	v_fmamk_f32 v9, v21, 0x3fb8aa3b, v30
	v_exp_f32_e32 v9, v9
	v_add_f32_e32 v10, v6, v10
	v_add_f32_e32 v10, v7, v10
	v_add_f32_e32 v10, v8, v10
	v_add_f32_e32 v14, v9, v10
	v_fmamk_f32 v10, v22, 0x3fb8aa3b, v30
	v_exp_f32_e32 v10, v10
	v_fmamk_f32 v11, v23, 0x3fb8aa3b, v30
	v_exp_f32_e32 v11, v11
	v_fmamk_f32 v12, v24, 0x3fb8aa3b, v30
	v_exp_f32_e32 v12, v12
	v_fmamk_f32 v13, v25, 0x3fb8aa3b, v30
	v_exp_f32_e32 v13, v13
	v_add_f32_e32 v14, v10, v14
	v_add_f32_e32 v14, v11, v14
	v_add_f32_e32 v14, v12, v14
	v_add_f32_e32 v18, v13, v14
	v_fmamk_f32 v14, v26, 0x3fb8aa3b, v30
	v_exp_f32_e32 v14, v14
	v_fmamk_f32 v15, v27, 0x3fb8aa3b, v30
	v_exp_f32_e32 v15, v15
	v_fmamk_f32 v16, v28, 0x3fb8aa3b, v30
	v_exp_f32_e32 v16, v16
	v_fmac_f32_e32 v30, 0x3fb8aa3b, v29
	v_exp_f32_e32 v17, v30
	v_add_f32_e32 v18, v14, v18
	v_add_f32_e32 v18, v15, v18
	v_add_f32_e32 v18, v16, v18
	v_add_f32_e32 v19, v17, v18
	v_mov_b32_e32 v20, v19
	s_nop 1
	v_permlane16_swap_b32_e32 v19, v20
	v_add_f32_e32 v19, v19, v20
	v_or_b32_e32 v18, 0xc0, v199
	v_mov_b32_e32 v20, v19
	s_nop 1
	v_permlane32_swap_b32_e32 v19, v20
	v_cmp_gt_u32_e32 vcc, s4, v18
	s_and_saveexec_b64 s[4:5], vcc
	s_cbranch_execz .LBB0_122
	v_add_f32_e32 v19, v19, v20
	v_rcp_f32_e32 v20, v19
	v_lshl_add_u32 v18, v18, 3, v186
	v_pk_mul_f32 v[2:3], v[20:21], v[2:3] op_sel_hi:[0,1]
	v_pk_mul_f32 v[4:5], v[20:21], v[4:5] op_sel_hi:[0,1]
	v_cvt_pk_f16_f32 v2, v2, v3
	v_cvt_pk_f16_f32 v3, v4, v5
	ds_write_b64 v18, v[2:3]
	v_pk_mul_f32 v[2:3], v[20:21], v[6:7] op_sel_hi:[0,1]
	v_pk_mul_f32 v[4:5], v[20:21], v[8:9] op_sel_hi:[0,1]
	v_cvt_pk_f16_f32 v2, v2, v3
	v_cvt_pk_f16_f32 v3, v4, v5
	ds_write_b64 v18, v[2:3] offset:6464
	v_pk_mul_f32 v[2:3], v[20:21], v[10:11] op_sel_hi:[0,1]
	v_pk_mul_f32 v[4:5], v[20:21], v[12:13] op_sel_hi:[0,1]
	v_cvt_pk_f16_f32 v2, v2, v3
	v_cvt_pk_f16_f32 v3, v4, v5
	ds_write_b64 v18, v[2:3] offset:12928
	v_pk_mul_f32 v[2:3], v[20:21], v[14:15] op_sel_hi:[0,1]
	v_pk_mul_f32 v[4:5], v[20:21], v[16:17] op_sel_hi:[0,1]
	v_cvt_pk_f16_f32 v2, v2, v3
	v_cvt_pk_f16_f32 v3, v4, v5
	ds_write_b64 v18, v[2:3] offset:19392
